# k_bscatter fetches all kernel arguments once at entry; k_bcount issues its edge loads before the LDS-zero barrier
# baseline (speedup 1.0000x reference)
.LBB0_10:
	s_or_b64 exec, exec, s[6:7]
	s_mul_i32 s3, s2, 0xc35
	v_add_u32_e32 v2, s3, v0
	v_mov_b32_e32 v3, 0
	v_add_u32_e32 v6, 0x400, v2
	v_mov_b32_e32 v7, v3
	s_waitcnt lgkmcnt(0)
	v_lshl_add_u64 v[18:19], v[6:7], 2, s[8:9]
	v_add_u32_e32 v6, 0x500, v2
	v_lshl_add_u64 v[20:21], v[6:7], 2, s[8:9]
	v_add_u32_e32 v6, 0x600, v2
	v_lshl_add_u64 v[16:17], v[2:3], 2, s[8:9]
	v_lshl_add_u64 v[22:23], v[6:7], 2, s[8:9]
	v_add_u32_e32 v6, 0x700, v2
	v_lshl_add_u64 v[24:25], v[6:7], 2, s[8:9]
	global_load_dword v15, v[16:17], off
	global_load_dword v14, v[16:17], off offset:1024
	global_load_dword v13, v[16:17], off offset:2048
	global_load_dword v12, v[16:17], off offset:3072
	global_load_dword v11, v[18:19], off
	global_load_dword v10, v[20:21], off
	global_load_dword v9, v[22:23], off
	global_load_dword v7, v[24:25], off
	v_add_u32_e32 v16, 0x800, v2
	v_mov_b32_e32 v17, v3
	v_lshl_add_u64 v[16:17], v[16:17], 2, s[8:9]
	global_load_dword v6, v[16:17], off
	s_movk_i32 s4, 0x335
	v_cmp_gt_u32_e32 vcc, s4, v0
	v_mov_b32_e32 v1, -1
	v_mov_b32_e32 v5, -1
	s_and_saveexec_b64 s[4:5], vcc
	s_cbranch_execz .LBB0_12
	v_add_u32_e32 v16, 0x900, v2
	v_mov_b32_e32 v17, v3
	v_lshl_add_u64 v[16:17], v[16:17], 2, s[8:9]
	global_load_dword v5, v[16:17], off

.LBB0_16:
	s_or_b64 exec, exec, s[4:5]
	s_barrier
	v_or_b32_e32 v2, 0xc00, v0
	s_movk_i32 s4, 0xc35
	v_cmp_gt_u32_e32 vcc, s4, v2
	s_and_saveexec_b64 s[4:5], vcc
	s_cbranch_execnz .LBB0_39
	s_or_b64 exec, exec, s[4:5]
	s_waitcnt vmcnt(8)
	v_cmp_lt_i32_e32 vcc, -1, v15
	s_and_saveexec_b64 s[4:5], vcc
	s_cbranch_execnz .LBB0_40

_Z10k_bscatterPKfPKiS2_S2_PiP15HIP_vector_typeIfLj2EEPf:
	s_load_dwordx8 s[20:27], s[0:1], 0x0
	s_load_dwordx4 s[28:31], s[0:1], 0x20
	s_cmp_lg_u32 s2, 1
	s_mov_b32 s7, 1
	s_cbranch_scc1 .LBB1_8
	s_load_dwordx2 s[8:9], s[0:1], 0x30
	v_sub_u32_e32 v1, 0x197f, v0
	v_lshrrev_b32_e32 v2, 9, v1
	v_add_u32_e32 v1, 2, v2
	v_and_b32_e32 v8, 30, v1
	s_mov_b32 s6, 0
	v_or_b32_e32 v1, 0x200, v0
	v_mov_b32_e32 v3, v2
	s_mov_b64 s[10:11], 0
	v_mov_b32_e32 v5, 0
	s_mov_b32 s12, s6
	v_mov_b64_e32 v[6:7], v[0:1]
	s_branch .LBB1_3

.LBB1_8:
	s_waitcnt lgkmcnt(0)
	s_mov_b64 s[6:7], s[24:25]
	s_mov_b64 s[8:9], s[20:21]
	s_mov_b64 s[10:11], s[22:23]
	s_movk_i32 s3, 0x187
	v_cmp_gt_u32_e32 vcc, s3, v0
	v_lshlrev_b32_e32 v23, 2, v0
	s_and_saveexec_b64 s[4:5], vcc
	v_mov_b32_e32 v1, 0
	ds_write_b32 v23, v1 offset:17664
	s_or_b64 exec, exec, s[4:5]
	s_mul_i32 s3, s2, 0xc35
	v_add_u32_e32 v4, s3, v0
	v_ashrrev_i32_e32 v5, 31, v4
	v_lshlrev_b64 v[2:3], 2, v[4:5]
	v_lshl_add_u64 v[6:7], s[6:7], 0, v[2:3]
	s_waitcnt lgkmcnt(0)
	v_lshl_add_u64 v[10:11], s[10:11], 0, v[2:3]
	v_lshl_add_u64 v[2:3], s[8:9], 0, v[2:3]
	global_load_dword v21, v[6:7], off
	global_load_dword v19, v[6:7], off offset:2048
	global_load_dword v8, v[10:11], off
	global_load_dword v1, v[10:11], off offset:2048
	global_load_dword v24, v[2:3], off
	global_load_dword v22, v[2:3], off offset:2048
	v_add_u32_e32 v2, 0x400, v4
	v_ashrrev_i32_e32 v3, 31, v2
	v_lshlrev_b64 v[6:7], 2, v[2:3]
	v_lshl_add_u64 v[2:3], s[6:7], 0, v[6:7]
	global_load_dword v17, v[2:3], off
	v_lshl_add_u64 v[2:3], s[10:11], 0, v[6:7]
	v_lshl_add_u64 v[6:7], s[8:9], 0, v[6:7]
	global_load_dword v20, v[6:7], off
	v_add_u32_e32 v6, 0x600, v4
	v_ashrrev_i32_e32 v7, 31, v6
	v_lshlrev_b64 v[6:7], 2, v[6:7]
	v_lshl_add_u64 v[10:11], s[6:7], 0, v[6:7]
	v_add_u32_e32 v4, 0x800, v4
	global_load_dword v15, v[10:11], off
	v_lshl_add_u64 v[10:11], s[10:11], 0, v[6:7]
	v_lshl_add_u64 v[6:7], s[8:9], 0, v[6:7]
	v_ashrrev_i32_e32 v5, 31, v4
	global_load_dword v16, v[6:7], off
	v_lshlrev_b64 v[6:7], 2, v[4:5]
	v_lshl_add_u64 v[4:5], s[6:7], 0, v[6:7]
	global_load_dword v9, v[4:5], off
	v_lshl_add_u64 v[4:5], s[10:11], 0, v[6:7]
	v_lshl_add_u64 v[6:7], s[8:9], 0, v[6:7]
	global_load_dword v2, v[2:3], off
	s_movk_i32 s4, 0x234
	global_load_dword v3, v[10:11], off
	global_load_dword v14, v[6:7], off
	v_cmp_lt_u32_e32 vcc, s4, v0
	global_load_dword v4, v[4:5], off
	v_or_b32_e32 v5, 0xa00, v0
	s_movk_i32 s4, 0x235
	v_add_u32_e32 v10, s3, v5
	v_cmp_gt_u32_e64 s[4:5], s4, v0
	v_mov_b32_e32 v7, -1
	v_ashrrev_i32_e32 v11, 31, v10
	s_and_saveexec_b64 s[12:13], s[4:5]
	s_cbranch_execz .LBB1_12
	v_lshl_add_u64 v[6:7], v[10:11], 2, s[6:7]
	global_load_dword v7, v[6:7], off

.LBB1_20:
	s_or_b64 exec, exec, s[4:5]
	v_and_b32_e32 v10, 0x7f, v0
	s_movk_i32 s3, 0x31
	v_cmp_gt_u32_e32 vcc, s3, v10
	s_and_saveexec_b64 s[6:7], vcc
	s_cbranch_execz .LBB1_22
	s_mov_b64 s[4:5], s[26:27]
	v_lshrrev_b32_e32 v25, 7, v0
	v_lshlrev_b32_e32 v29, 5, v10
	v_lshlrev_b32_e32 v28, 4, v10
	s_movk_i32 s3, 0x620
	v_readfirstlane_b32 s12, v0
	v_mad_u32_u24 v25, v25, s3, v29
	s_lshr_b32 s12, s12, 7
	s_lshl_b32 s13, s12, 6
	s_mul_i32 s14, s13, 0x310
	s_sub_i32 s15, s2, s13
	v_mov_b32_e32 v30, 0
	v_mov_b32_e32 v31, 0
	v_mov_b32_e32 v32, 0
	v_mov_b32_e32 v33, 0
	v_mov_b32_e32 v34, 0
	v_mov_b32_e32 v35, 0
	v_mov_b32_e32 v36, 0
	v_mov_b32_e32 v37, 0
	v_mov_b32_e32 v38, 0
	v_mov_b32_e32 v39, 0
	v_mov_b32_e32 v40, 0
	v_mov_b32_e32 v41, 0
	v_mov_b32_e32 v42, 0
	v_mov_b32_e32 v43, 0
	v_mov_b32_e32 v44, 0
	v_mov_b32_e32 v45, 0
	s_waitcnt lgkmcnt(0)
	s_add_u32 s4, s4, s14
	s_addc_u32 s5, s5, 0
	global_load_dwordx4 v[68:71], v28, s[4:5]
	global_load_dwordx4 v[72:75], v28, s[4:5] offset:784
	global_load_dwordx4 v[76:79], v28, s[4:5] offset:1568
	global_load_dwordx4 v[80:83], v28, s[4:5] offset:2352
	global_load_dwordx4 v[84:87], v28, s[4:5] offset:3136
	s_add_u32 s4, s4, 0xf50
	s_addc_u32 s5, s5, 0
	global_load_dwordx4 v[88:91], v28, s[4:5]
	global_load_dwordx4 v[92:95], v28, s[4:5] offset:784
	global_load_dwordx4 v[96:99], v28, s[4:5] offset:1568
	global_load_dwordx4 v[100:103], v28, s[4:5] offset:2352
	global_load_dwordx4 v[104:107], v28, s[4:5] offset:3136
	s_add_u32 s4, s4, 0xf50
	s_addc_u32 s5, s5, 0
	global_load_dwordx4 v[108:111], v28, s[4:5]
	global_load_dwordx4 v[112:115], v28, s[4:5] offset:784
	global_load_dwordx4 v[116:119], v28, s[4:5] offset:1568
	global_load_dwordx4 v[120:123], v28, s[4:5] offset:2352
	global_load_dwordx4 v[124:127], v28, s[4:5] offset:3136
	s_add_u32 s4, s4, 0xf50
	s_addc_u32 s5, s5, 0
	global_load_dwordx4 v[128:131], v28, s[4:5]
	global_load_dwordx4 v[132:135], v28, s[4:5] offset:784
	global_load_dwordx4 v[136:139], v28, s[4:5] offset:1568
	global_load_dwordx4 v[140:143], v28, s[4:5] offset:2352
	global_load_dwordx4 v[144:147], v28, s[4:5] offset:3136
	s_add_u32 s4, s4, 0xf50
	s_addc_u32 s5, s5, 0
	global_load_dwordx4 v[148:151], v28, s[4:5]
	global_load_dwordx4 v[152:155], v28, s[4:5] offset:784
	global_load_dwordx4 v[156:159], v28, s[4:5] offset:1568
	global_load_dwordx4 v[160:163], v28, s[4:5] offset:2352
	global_load_dwordx4 v[164:167], v28, s[4:5] offset:3136
	s_add_u32 s4, s4, 0xf50
	s_addc_u32 s5, s5, 0
	global_load_dwordx4 v[168:171], v28, s[4:5]
	global_load_dwordx4 v[172:175], v28, s[4:5] offset:784
	global_load_dwordx4 v[176:179], v28, s[4:5] offset:1568
	global_load_dwordx4 v[180:183], v28, s[4:5] offset:2352
	global_load_dwordx4 v[184:187], v28, s[4:5] offset:3136
	s_add_u32 s4, s4, 0xf50
	s_addc_u32 s5, s5, 0
	global_load_dwordx4 v[188:191], v28, s[4:5]
	global_load_dwordx4 v[192:195], v28, s[4:5] offset:784
	s_waitcnt vmcnt(16)
	v_add3_u32 v46, v68, v72, v76
	v_add3_u32 v46, v46, v80, v84
	v_add3_u32 v46, v46, v88, v92
	v_add3_u32 v46, v46, v96, v100
	v_add3_u32 v46, v46, v104, v108
	v_add3_u32 v46, v46, v112, v116
	v_add3_u32 v46, v46, v120, v124
	v_add_u32_e32 v46, v46, v128
	v_add3_u32 v47, v69, v73, v77
	v_add3_u32 v47, v47, v81, v85
	v_add3_u32 v47, v47, v89, v93
	v_add3_u32 v47, v47, v97, v101
	v_add3_u32 v47, v47, v105, v109
	v_add3_u32 v47, v47, v113, v117
	v_add3_u32 v47, v47, v121, v125
	v_add_u32_e32 v47, v47, v129
	v_add3_u32 v48, v70, v74, v78
	v_add3_u32 v48, v48, v82, v86
	v_add3_u32 v48, v48, v90, v94
	v_add3_u32 v48, v48, v98, v102
	v_add3_u32 v48, v48, v106, v110
	v_add3_u32 v48, v48, v114, v118
	v_add3_u32 v48, v48, v122, v126
	v_add_u32_e32 v48, v48, v130
	v_add3_u32 v49, v71, v75, v79
	v_add3_u32 v49, v49, v83, v87
	v_add3_u32 v49, v49, v91, v95
	v_add3_u32 v49, v49, v99, v103
	v_add3_u32 v49, v49, v107, v111
	v_add3_u32 v49, v49, v115, v119
	v_add3_u32 v49, v49, v123, v127
	v_add_u32_e32 v49, v49, v131
	v_and_b32_e32 v50, 0xffff, v46
	v_lshrrev_b32_e32 v51, 16, v46
	v_and_b32_e32 v52, 0xffff, v47
	v_lshrrev_b32_e32 v53, 16, v47
	v_and_b32_e32 v54, 0xffff, v48
	v_lshrrev_b32_e32 v55, 16, v48
	v_and_b32_e32 v56, 0xffff, v49
	v_lshrrev_b32_e32 v57, 16, v49
	v_add_u32_e32 v30, v30, v50
	v_add_u32_e32 v31, v31, v51
	v_add_u32_e32 v32, v32, v52
	v_add_u32_e32 v33, v33, v53
	v_add_u32_e32 v34, v34, v54
	v_add_u32_e32 v35, v35, v55
	v_add_u32_e32 v36, v36, v56
	v_add_u32_e32 v37, v37, v57
	s_cmp_ge_i32 s15, 16
	s_cbranch_scc0 .Lbscat_nf_0
	v_add_u32_e32 v38, v38, v50
	v_add_u32_e32 v39, v39, v51
	v_add_u32_e32 v40, v40, v52
	v_add_u32_e32 v41, v41, v53
	v_add_u32_e32 v42, v42, v54
	v_add_u32_e32 v43, v43, v55
	v_add_u32_e32 v44, v44, v56
	v_add_u32_e32 v45, v45, v57
	s_branch .Lbscat_dn_0

.LBB1_60:
	s_or_b64 exec, exec, s[4:5]
	s_barrier
	s_and_saveexec_b64 s[4:5], vcc
	v_add_u32_e32 v11, v10, v11
	ds_write_b64 v12, v[10:11] offset:13568
	s_or_b64 exec, exec, s[4:5]
	s_mov_b64 s[12:13], s[30:31]
	s_cmp_eq_u32 s2, 0
	s_movk_i32 s4, 0x188
	s_cselect_b64 s[2:3], -1, 0
	v_cmp_gt_u32_e32 vcc, s4, v0
	s_and_b64 s[4:5], s[2:3], vcc
	s_waitcnt lgkmcnt(0)
	s_barrier
	s_and_saveexec_b64 s[2:3], s[4:5]
	s_cbranch_execz .LBB1_66
	s_mov_b64 s[0:1], s[28:29]
	s_movk_i32 s4, 0x187
	v_cmp_ne_u32_e32 vcc, s4, v0
	v_mov_b32_e32 v0, 0xc3500
	s_and_saveexec_b64 s[4:5], vcc
	ds_read_b32 v0, v13 offset:1024
	s_or_b64 exec, exec, s[4:5]
	s_waitcnt lgkmcnt(0)
	global_store_dword v23, v0, s[0:1]

	.amdhsa_kernel _Z10k_bscatterPKfPKiS2_S2_PiP15HIP_vector_typeIfLj2EEPf
		.amdhsa_group_segment_fixed_size 19228
		.amdhsa_private_segment_fixed_size 0
		.amdhsa_kernarg_size 56
		.amdhsa_user_sgpr_count 2
		.amdhsa_user_sgpr_dispatch_ptr 0
		.amdhsa_user_sgpr_queue_ptr 0
		.amdhsa_user_sgpr_kernarg_segment_ptr 1
		.amdhsa_user_sgpr_dispatch_id 0
		.amdhsa_user_sgpr_kernarg_preload_length 0
		.amdhsa_user_sgpr_kernarg_preload_offset 0
		.amdhsa_user_sgpr_private_segment_size 0
		.amdhsa_uses_dynamic_stack 0
		.amdhsa_enable_private_segment 0
		.amdhsa_system_sgpr_workgroup_id_x 1
		.amdhsa_system_sgpr_workgroup_id_y 0
		.amdhsa_system_sgpr_workgroup_id_z 0
		.amdhsa_system_sgpr_workgroup_info 0
		.amdhsa_system_vgpr_workitem_id 0
		.amdhsa_next_free_vgpr 196
		.amdhsa_next_free_sgpr 32
		.amdhsa_accum_offset 196
		.amdhsa_reserve_vcc 1
		.amdhsa_float_round_mode_32 0
		.amdhsa_float_round_mode_16_64 0
		.amdhsa_float_denorm_mode_32 3
		.amdhsa_float_denorm_mode_16_64 3
		.amdhsa_dx10_clamp 1
		.amdhsa_ieee_mode 1
		.amdhsa_fp16_overflow 0
		.amdhsa_tg_split 0
		.amdhsa_exception_fp_ieee_invalid_op 0
		.amdhsa_exception_fp_denorm_src 0
		.amdhsa_exception_fp_ieee_div_zero 0
		.amdhsa_exception_fp_ieee_overflow 0
		.amdhsa_exception_fp_ieee_underflow 0
		.amdhsa_exception_fp_ieee_inexact 0
		.amdhsa_exception_int_div_zero 0
	.end_amdhsa_kernel

amdhsa.kernels:
  - .agpr_count:     0
    .args:
      - .actual_access:  read_only
        .address_space:  global
        .offset:         0
        .size:           8
        .value_kind:     global_buffer
      - .actual_access:  write_only
        .address_space:  global
        .offset:         8
        .size:           8
        .value_kind:     global_buffer
      - .offset:         16
        .size:           288
        .value_kind:     by_value
      - .actual_access:  write_only
        .address_space:  global
        .offset:         304
        .size:           8
        .value_kind:     global_buffer
      - .actual_access:  write_only
        .address_space:  global
        .offset:         312
        .size:           8
        .value_kind:     global_buffer
    .group_segment_fixed_size: 1564
    .kernarg_segment_align: 8
    .kernarg_segment_size: 320
    .language:       OpenCL C
    .language_version:
      - 2
      - 0
    .max_flat_workgroup_size: 256
    .name:           _Z8k_bcountPKiPi8PrepArgsPDF16_S3_
    .private_segment_fixed_size: 0
    .sgpr_count:     26
    .sgpr_spill_count: 0
    .symbol:         _Z8k_bcountPKiPi8PrepArgsPDF16_S3_.kd
    .uniform_work_group_size: 1
    .uses_dynamic_stack: false
    .vgpr_count:     26
    .vgpr_spill_count: 0
    .wavefront_size: 64
  - .agpr_count:     0
    .args:
      - .actual_access:  read_only
        .address_space:  global
        .offset:         0
        .size:           8
        .value_kind:     global_buffer
      - .actual_access:  read_only
        .address_space:  global
        .offset:         8
        .size:           8
        .value_kind:     global_buffer
      - .actual_access:  read_only
        .address_space:  global
        .offset:         16
        .size:           8
        .value_kind:     global_buffer
      - .actual_access:  read_only
        .address_space:  global
        .offset:         24
        .size:           8
        .value_kind:     global_buffer
      - .actual_access:  write_only
        .address_space:  global
        .offset:         32
        .size:           8
        .value_kind:     global_buffer
      - .actual_access:  write_only
        .address_space:  global
        .offset:         40
        .size:           8
        .value_kind:     global_buffer
      - .actual_access:  write_only
        .address_space:  global
        .offset:         48
        .size:           8
        .value_kind:     global_buffer
    .group_segment_fixed_size: 19228
    .kernarg_segment_align: 8
    .kernarg_segment_size: 56
    .language:       OpenCL C
    .language_version:
      - 2
      - 0
    .max_flat_workgroup_size: 512
    .name:           _Z10k_bscatterPKfPKiS2_S2_PiP15HIP_vector_typeIfLj2EEPf
    .private_segment_fixed_size: 0
    .sgpr_count:     38
    .sgpr_spill_count: 0
    .symbol:         _Z10k_bscatterPKfPKiS2_S2_PiP15HIP_vector_typeIfLj2EEPf.kd
    .uniform_work_group_size: 1
    .uses_dynamic_stack: false
    .vgpr_count:     196
    .vgpr_spill_count: 0
    .wavefront_size: 64
  - .agpr_count:     0
    .args:
      - .actual_access:  read_only
        .address_space:  global
        .offset:         0
        .size:           8
        .value_kind:     global_buffer
      - .actual_access:  read_only
        .address_space:  global
        .offset:         8
        .size:           8
        .value_kind:     global_buffer
      - .actual_access:  read_only
        .address_space:  global
        .offset:         16
        .size:           8
        .value_kind:     global_buffer
      - .actual_access:  write_only
        .address_space:  global
        .offset:         24
        .size:           8
        .value_kind:     global_buffer
      - .actual_access:  write_only
        .address_space:  global
        .offset:         32
        .size:           8
        .value_kind:     global_buffer
    .group_segment_fixed_size: 1024
    .kernarg_segment_align: 8
    .kernarg_segment_size: 40
    .language:       OpenCL C
    .language_version:
      - 2
      - 0
    .max_flat_workgroup_size: 512
    .name:           _Z7k_bsortPK15HIP_vector_typeIfLj2EEPKiS4_PS_IfLj4EEPi
    .private_segment_fixed_size: 0
    .sgpr_count:     58
    .sgpr_spill_count: 0
    .symbol:         _Z7k_bsortPK15HIP_vector_typeIfLj2EEPKiS4_PS_IfLj4EEPi.kd
    .uniform_work_group_size: 1
    .uses_dynamic_stack: false
    .vgpr_count:     71
    .vgpr_spill_count: 0
    .wavefront_size: 64
  - .agpr_count:     0
    .args:
      - .actual_access:  read_only
        .address_space:  global
        .offset:         0
        .size:           8
        .value_kind:     global_buffer
      - .actual_access:  read_only
        .address_space:  global
        .offset:         8
        .size:           8
        .value_kind:     global_buffer
      - .actual_access:  read_only
        .address_space:  global
        .offset:         16
        .size:           8
        .value_kind:     global_buffer
      - .actual_access:  read_only
        .address_space:  global
        .offset:         24
        .size:           8
        .value_kind:     global_buffer
      - .actual_access:  read_only
        .address_space:  global
        .offset:         32
        .size:           8
        .value_kind:     global_buffer
      - .actual_access:  read_only
        .address_space:  global
        .offset:         40
        .size:           8
        .value_kind:     global_buffer
      - .actual_access:  write_only
        .address_space:  global
        .offset:         48
        .size:           8
        .value_kind:     global_buffer
      - .actual_access:  write_only
        .address_space:  global
        .offset:         56
        .size:           8
        .value_kind:     global_buffer
      - .offset:         64
        .size:           4
        .value_kind:     hidden_block_count_x
      - .offset:         68
        .size:           4
        .value_kind:     hidden_block_count_y
      - .offset:         72
        .size:           4
        .value_kind:     hidden_block_count_z
      - .offset:         76
        .size:           2
        .value_kind:     hidden_group_size_x
      - .offset:         78
        .size:           2
        .value_kind:     hidden_group_size_y
      - .offset:         80
        .size:           2
        .value_kind:     hidden_group_size_z
      - .offset:         82
        .size:           2
        .value_kind:     hidden_remainder_x
      - .offset:         84
        .size:           2
        .value_kind:     hidden_remainder_y
      - .offset:         86
        .size:           2
        .value_kind:     hidden_remainder_z
      - .offset:         104
        .size:           8
        .value_kind:     hidden_global_offset_x
      - .offset:         112
        .size:           8
        .value_kind:     hidden_global_offset_y
      - .offset:         120
        .size:           8
        .value_kind:     hidden_global_offset_z
      - .offset:         128
        .size:           2
        .value_kind:     hidden_grid_dims
    .group_segment_fixed_size: 31488
    .kernarg_segment_align: 8
    .kernarg_segment_size: 320
    .language:       OpenCL C
    .language_version:
      - 2
      - 0
    .max_flat_workgroup_size: 256
    .name:           _Z7k_edge0PK15HIP_vector_typeIfLj4EEPKDv8_DF16_S5_PKfS7_S7_PfS8_
    .private_segment_fixed_size: 0
    .sgpr_count:     59
    .sgpr_spill_count: 0
    .symbol:         _Z7k_edge0PK15HIP_vector_typeIfLj4EEPKDv8_DF16_S5_PKfS7_S7_PfS8_.kd
    .uniform_work_group_size: 1
    .uses_dynamic_stack: false
    .vgpr_count:     98
    .vgpr_spill_count: 0
    .wavefront_size: 64
  - .agpr_count:     0
    .args:
      - .actual_access:  read_only
        .address_space:  global
        .offset:         0
        .size:           8
        .value_kind:     global_buffer
      - .actual_access:  read_only
        .address_space:  global
        .offset:         8
        .size:           8
        .value_kind:     global_buffer
      - .actual_access:  read_only
        .address_space:  global
        .offset:         16
        .size:           8
        .value_kind:     global_buffer
      - .actual_access:  read_only
        .address_space:  global
        .offset:         24
        .size:           8
        .value_kind:     global_buffer
      - .actual_access:  read_only
        .address_space:  global
        .offset:         32
        .size:           8
        .value_kind:     global_buffer
      - .actual_access:  read_only
        .address_space:  global
        .offset:         40
        .size:           8
        .value_kind:     global_buffer
      - .address_space:  global
        .offset:         48
        .size:           8
        .value_kind:     global_buffer
      - .actual_access:  write_only
        .address_space:  global
        .offset:         56
        .size:           8
        .value_kind:     global_buffer
      - .actual_access:  write_only
        .address_space:  global
        .offset:         64
        .size:           8
        .value_kind:     global_buffer
      - .offset:         72
        .size:           4
        .value_kind:     hidden_block_count_x
      - .offset:         76
        .size:           4
        .value_kind:     hidden_block_count_y
      - .offset:         80
        .size:           4
        .value_kind:     hidden_block_count_z
      - .offset:         84
        .size:           2
        .value_kind:     hidden_group_size_x
      - .offset:         86
        .size:           2
        .value_kind:     hidden_group_size_y
      - .offset:         88
        .size:           2
        .value_kind:     hidden_group_size_z
      - .offset:         90
        .size:           2
        .value_kind:     hidden_remainder_x
      - .offset:         92
        .size:           2
        .value_kind:     hidden_remainder_y
      - .offset:         94
        .size:           2
        .value_kind:     hidden_remainder_z
      - .offset:         112
        .size:           8
        .value_kind:     hidden_global_offset_x
      - .offset:         120
        .size:           8
        .value_kind:     hidden_global_offset_y
      - .offset:         128
        .size:           8
        .value_kind:     hidden_global_offset_z
      - .offset:         136
        .size:           2
        .value_kind:     hidden_grid_dims
    .group_segment_fixed_size: 31488
    .kernarg_segment_align: 8
    .kernarg_segment_size: 328
    .language:       OpenCL C
    .language_version:
      - 2
      - 0
    .max_flat_workgroup_size: 256
    .name:           _Z7k_edge1PK15HIP_vector_typeIfLj4EEPKDv8_DF16_S5_PKfS7_S7_PKDv2_DF16_PfSB_
    .private_segment_fixed_size: 0
    .sgpr_count:     56
    .sgpr_spill_count: 0
    .symbol:         _Z7k_edge1PK15HIP_vector_typeIfLj4EEPKDv8_DF16_S5_PKfS7_S7_PKDv2_DF16_PfSB_.kd
    .uniform_work_group_size: 1
    .uses_dynamic_stack: false
    .vgpr_count:     128
    .vgpr_spill_count: 0
    .wavefront_size: 64
  - .agpr_count:     0
    .args:
      - .actual_access:  read_only
        .address_space:  global
        .offset:         0
        .size:           8
        .value_kind:     global_buffer
      - .actual_access:  read_only
        .address_space:  global
        .offset:         8
        .size:           8
        .value_kind:     global_buffer
      - .address_space:  global
        .offset:         16
        .size:           8
        .value_kind:     global_buffer
      - .address_space:  global
        .offset:         24
        .size:           8
        .value_kind:     global_buffer
    .group_segment_fixed_size: 0
    .kernarg_segment_align: 8
    .kernarg_segment_size: 32
    .language:       OpenCL C
    .language_version:
      - 2
      - 0
    .max_flat_workgroup_size: 256
    .name:           _Z6k_poolPKfPKiPfS3_
    .private_segment_fixed_size: 0
    .sgpr_count:     20
    .sgpr_spill_count: 0
    .symbol:         _Z6k_poolPKfPKiPfS3_.kd
    .uniform_work_group_size: 1
    .uses_dynamic_stack: false
    .vgpr_count:     16
    .vgpr_spill_count: 0
    .wavefront_size: 64
  - .agpr_count:     0
    .args:
      - .actual_access:  read_only
        .address_space:  global
        .offset:         0
        .size:           8
        .value_kind:     global_buffer
      - .actual_access:  read_only
        .address_space:  global
        .offset:         8
        .size:           8
        .value_kind:     global_buffer
      - .actual_access:  read_only
        .address_space:  global
        .offset:         16
        .size:           8
        .value_kind:     global_buffer
      - .actual_access:  read_only
        .address_space:  global
        .offset:         24
        .size:           8
        .value_kind:     global_buffer
      - .actual_access:  read_only
        .address_space:  global
        .offset:         32
        .size:           8
        .value_kind:     global_buffer
      - .actual_access:  read_only
        .address_space:  global
        .offset:         40
        .size:           8
        .value_kind:     global_buffer
      - .actual_access:  write_only
        .address_space:  global
        .offset:         48
        .size:           8
        .value_kind:     global_buffer
    .group_segment_fixed_size: 20480
    .kernarg_segment_align: 8
    .kernarg_segment_size: 56
    .language:       OpenCL C
    .language_version:
      - 2
      - 0
    .max_flat_workgroup_size: 64
    .name:           _Z7k_finalPKfS0_S0_S0_S0_S0_Pf
    .private_segment_fixed_size: 0
    .sgpr_count:     42
    .sgpr_spill_count: 0
    .symbol:         _Z7k_finalPKfS0_S0_S0_S0_S0_Pf.kd
    .uniform_work_group_size: 1
    .uses_dynamic_stack: false
    .vgpr_count:     144
    .vgpr_spill_count: 0
    .wavefront_size: 64
  - .agpr_count:     0
    .args:
      - .actual_access:  read_only
        .address_space:  global
        .offset:         0
        .size:           8
        .value_kind:     global_buffer
      - .address_space:  global
        .offset:         8
        .size:           8
        .value_kind:     global_buffer
      - .address_space:  global
        .offset:         16
        .size:           8
        .value_kind:     global_buffer
      - .actual_access:  read_only
        .address_space:  global
        .offset:         24
        .size:           8
        .value_kind:     global_buffer
      - .actual_access:  read_only
        .address_space:  global
        .offset:         32
        .size:           8
        .value_kind:     global_buffer
      - .actual_access:  read_only
        .address_space:  global
        .offset:         40
        .size:           8
        .value_kind:     global_buffer
      - .actual_access:  read_only
        .address_space:  global
        .offset:         48
        .size:           8
        .value_kind:     global_buffer
      - .actual_access:  read_only
        .address_space:  global
        .offset:         56
        .size:           8
        .value_kind:     global_buffer
      - .actual_access:  read_only
        .address_space:  global
        .offset:         64
        .size:           8
        .value_kind:     global_buffer
      - .actual_access:  read_only
        .address_space:  global
        .offset:         72
        .size:           8
        .value_kind:     global_buffer
      - .actual_access:  read_only
        .address_space:  global
        .offset:         80
        .size:           8
        .value_kind:     global_buffer
      - .actual_access:  read_only
        .address_space:  global
        .offset:         88
        .size:           8
        .value_kind:     global_buffer
      - .actual_access:  read_only
        .address_space:  global
        .offset:         96
        .size:           8
        .value_kind:     global_buffer
      - .actual_access:  read_only
        .address_space:  global
        .offset:         104
        .size:           8
        .value_kind:     global_buffer
      - .actual_access:  read_only
        .address_space:  global
        .offset:         112
        .size:           8
        .value_kind:     global_buffer
    .group_segment_fixed_size: 59392
    .kernarg_segment_align: 8
    .kernarg_segment_size: 120
    .language:       OpenCL C
    .language_version:
      - 2
      - 0
    .max_flat_workgroup_size: 256
    .name:           _Z6k_nodeILi0ELi0EEvPfS0_PDv2_DF16_PKiPKfS4_S0_S0_S4_S6_PKDv8_DF16_S6_S9_S6_S9_
    .private_segment_fixed_size: 0
    .sgpr_count:     30
    .sgpr_spill_count: 0
    .symbol:         _Z6k_nodeILi0ELi0EEvPfS0_PDv2_DF16_PKiPKfS4_S0_S0_S4_S6_PKDv8_DF16_S6_S9_S6_S9_.kd
    .uniform_work_group_size: 1
    .uses_dynamic_stack: false
    .vgpr_count:     154
    .vgpr_spill_count: 0
    .wavefront_size: 64
  - .agpr_count:     0
    .args:
      - .actual_access:  read_only
        .address_space:  global
        .offset:         0
        .size:           8
        .value_kind:     global_buffer
      - .address_space:  global
        .offset:         8
        .size:           8
        .value_kind:     global_buffer
      - .address_space:  global
        .offset:         16
        .size:           8
        .value_kind:     global_buffer
      - .actual_access:  read_only
        .address_space:  global
        .offset:         24
        .size:           8
        .value_kind:     global_buffer
      - .actual_access:  read_only
        .address_space:  global
        .offset:         32
        .size:           8
        .value_kind:     global_buffer
      - .actual_access:  read_only
        .address_space:  global
        .offset:         40
        .size:           8
        .value_kind:     global_buffer
      - .actual_access:  read_only
        .address_space:  global
        .offset:         48
        .size:           8
        .value_kind:     global_buffer
      - .actual_access:  read_only
        .address_space:  global
        .offset:         56
        .size:           8
        .value_kind:     global_buffer
      - .actual_access:  read_only
        .address_space:  global
        .offset:         64
        .size:           8
        .value_kind:     global_buffer
      - .actual_access:  read_only
        .address_space:  global
        .offset:         72
        .size:           8
        .value_kind:     global_buffer
      - .actual_access:  read_only
        .address_space:  global
        .offset:         80
        .size:           8
        .value_kind:     global_buffer
      - .actual_access:  read_only
        .address_space:  global
        .offset:         88
        .size:           8
        .value_kind:     global_buffer
      - .actual_access:  read_only
        .address_space:  global
        .offset:         96
        .size:           8
        .value_kind:     global_buffer
      - .actual_access:  read_only
        .address_space:  global
        .offset:         104
        .size:           8
        .value_kind:     global_buffer
      - .actual_access:  read_only
        .address_space:  global
        .offset:         112
        .size:           8
        .value_kind:     global_buffer
    .group_segment_fixed_size: 59392
    .kernarg_segment_align: 8
    .kernarg_segment_size: 120
    .language:       OpenCL C
    .language_version:
      - 2
      - 0
    .max_flat_workgroup_size: 256
    .name:           _Z6k_nodeILi1ELi0EEvPfS0_PDv2_DF16_PKiPKfS4_S0_S0_S4_S6_PKDv8_DF16_S6_S9_S6_S9_
    .private_segment_fixed_size: 0
    .sgpr_count:     30
    .sgpr_spill_count: 0
    .symbol:         _Z6k_nodeILi1ELi0EEvPfS0_PDv2_DF16_PKiPKfS4_S0_S0_S4_S6_PKDv8_DF16_S6_S9_S6_S9_.kd
    .uniform_work_group_size: 1
    .uses_dynamic_stack: false
    .vgpr_count:     220
    .vgpr_spill_count: 0
    .wavefront_size: 64
  - .agpr_count:     0
    .args:
      - .actual_access:  read_only
        .address_space:  global
        .offset:         0
        .size:           8
        .value_kind:     global_buffer
      - .actual_access:  read_only
        .address_space:  global
        .offset:         8
        .size:           8
        .value_kind:     global_buffer
      - .address_space:  global
        .offset:         16
        .size:           8
        .value_kind:     global_buffer
      - .actual_access:  read_only
        .address_space:  global
        .offset:         24
        .size:           8
        .value_kind:     global_buffer
      - .actual_access:  read_only
        .address_space:  global
        .offset:         32
        .size:           8
        .value_kind:     global_buffer
      - .actual_access:  read_only
        .address_space:  global
        .offset:         40
        .size:           8
        .value_kind:     global_buffer
      - .address_space:  global
        .offset:         48
        .size:           8
        .value_kind:     global_buffer
      - .address_space:  global
        .offset:         56
        .size:           8
        .value_kind:     global_buffer
      - .actual_access:  read_only
        .address_space:  global
        .offset:         64
        .size:           8
        .value_kind:     global_buffer
      - .actual_access:  read_only
        .address_space:  global
        .offset:         72
        .size:           8
        .value_kind:     global_buffer
      - .actual_access:  read_only
        .address_space:  global
        .offset:         80
        .size:           8
        .value_kind:     global_buffer
      - .actual_access:  read_only
        .address_space:  global
        .offset:         88
        .size:           8
        .value_kind:     global_buffer
      - .actual_access:  read_only
        .address_space:  global
        .offset:         96
        .size:           8
        .value_kind:     global_buffer
      - .actual_access:  read_only
        .address_space:  global
        .offset:         104
        .size:           8
        .value_kind:     global_buffer
      - .actual_access:  read_only
        .address_space:  global
        .offset:         112
        .size:           8
        .value_kind:     global_buffer
    .group_segment_fixed_size: 59392
    .kernarg_segment_align: 8
    .kernarg_segment_size: 120
    .language:       OpenCL C
    .language_version:
      - 2
      - 0
    .max_flat_workgroup_size: 256
    .name:           _Z6k_nodeILi1ELi1EEvPfS0_PDv2_DF16_PKiPKfS4_S0_S0_S4_S6_PKDv8_DF16_S6_S9_S6_S9_
    .private_segment_fixed_size: 0
    .sgpr_count:     30
    .sgpr_spill_count: 0
    .symbol:         _Z6k_nodeILi1ELi1EEvPfS0_PDv2_DF16_PKiPKfS4_S0_S0_S4_S6_PKDv8_DF16_S6_S9_S6_S9_.kd
    .uniform_work_group_size: 1
    .uses_dynamic_stack: false
    .vgpr_count:     220
    .vgpr_spill_count: 0
    .wavefront_size: 64
